# prep patches plus edge_main prologue without the 8 scratch stores (waits recounted)
# speedup vs baseline: 1.0097x; 1.0008x over previous
_Z9edge_mainPKfS0_PKiS2_PKcPcS0_S0_Pf:
	s_load_dwordx8 s[8:15], s[0:1], 0x0
	v_and_b32_e32 v2, 16, v0
	v_lshrrev_b32_e32 v1, 6, v0
	v_cmp_eq_u32_e32 vcc, 0, v2
	v_and_b32_e32 v106, 15, v0
	s_waitcnt lgkmcnt(0)
	v_mov_b32_e32 v3, s15
	v_mov_b32_e32 v4, s13
	v_cndmask_b32_e32 v95, v3, v4, vcc
	v_mov_b32_e32 v2, s14
	v_mov_b32_e32 v3, s12
	v_lshl_add_u32 v62, v1, 8, s2
	v_cndmask_b32_e32 v94, v2, v3, vcc
	v_lshl_or_b32 v2, v62, 4, v106
	v_ashrrev_i32_e32 v3, 31, v2
	v_lshl_add_u64 v[4:5], v[2:3], 2, v[94:95]
	v_add_u32_e32 v2, 0x8000, v2
	v_ashrrev_i32_e32 v3, 31, v2
	v_lshl_add_u64 v[2:3], v[2:3], 2, v[94:95]
	global_load_dword v60, v[4:5], off
	global_load_dword v64, v[2:3], off
	s_load_dwordx4 s[12:15], s[0:1], 0x20
	v_and_b32_e32 v70, 63, v0
	v_lshlrev_b32_e32 v68, 4, v70
	v_mov_b32_e32 v69, 0
	v_mov_b32_e32 v2, 0x30d40
	v_bfe_u32 v65, v0, 3, 3
	v_and_b32_e32 v66, 0x70, v68
	v_cndmask_b32_e64 v2, v2, 0, vcc
	v_mov_b32_e32 v3, v69
	v_mov_b32_e32 v67, v69
	s_waitcnt vmcnt(1)
	v_ashrrev_i32_e32 v61, 31, v60
	v_lshlrev_b32_e32 v58, 4, v0
	v_mov_b32_e32 v59, v69
	s_waitcnt lgkmcnt(0)
	v_lshl_add_u64 v[4:5], s[12:13], 0, v[58:59]
	s_movk_i32 s3, 0x2000
	v_add_co_u32_e32 v6, vcc, s3, v4
	s_movk_i32 s3, 0x6000
	s_nop 0
	v_addc_co_u32_e32 v7, vcc, 0, v5, vcc
	global_load_dwordx4 v[72:75], v58, s[12:13]
	v_or_b32_e32 v8, 0x4000, v58
	global_load_dwordx4 v[76:79], v[6:7], off
	global_load_dwordx4 v[80:83], v8, s[12:13]
	v_add_co_u32_e32 v6, vcc, s3, v4
	s_mov_b32 s3, 0xa000
	s_nop 0
	v_addc_co_u32_e32 v7, vcc, 0, v5, vcc
	v_or_b32_e32 v8, 0x8000, v58
	global_load_dwordx4 v[84:87], v[6:7], off
	global_load_dwordx4 v[88:91], v8, s[12:13]
	v_add_co_u32_e32 v6, vcc, s3, v4
	s_mov_b32 s3, 0xe000
	s_nop 0
	v_addc_co_u32_e32 v7, vcc, 0, v5, vcc
	v_lshl_add_u64 v[2:3], s[12:13], 0, v[2:3]
	s_mov_b64 s[4:5], 0x100000
	v_ashrrev_i32_e32 v63, 31, v62
	v_add_co_u32_e32 v4, vcc, s3, v4
	v_lshl_add_u64 v[96:97], v[2:3], 0, s[4:5]
	v_lshlrev_b64 v[2:3], 13, v[62:63]
	v_addc_co_u32_e32 v5, vcc, 0, v5, vcc
	v_lshl_add_u64 v[2:3], s[8:9], 0, v[2:3]
	v_or_b32_e32 v8, 0xc000, v58
	global_load_dwordx4 v[102:105], v[6:7], off
	global_load_dwordx4 v[110:113], v8, s[12:13]
	s_movk_i32 s3, 0x1000
	v_or_b32_e32 v6, 0x1200, v0
	v_cmp_gt_u32_e32 vcc, 32, v0
	v_lshl_add_u64 v[18:19], v[2:3], 0, v[68:69]
	v_add_co_u32_e64 v34, s[4:5], s3, v18
	v_cndmask_b32_e32 v6, 0, v6, vcc
	v_lshlrev_b32_e32 v6, 4, v6
	v_addc_co_u32_e64 v35, s[4:5], 0, v19, s[4:5]
	v_mbcnt_lo_u32_b32 v36, -1, 0
	global_load_dwordx4 v[114:117], v[4:5], off
	global_load_dwordx4 v[54:57], v6, s[12:13]
	s_nop 0
	global_load_dwordx4 v[2:5], v[18:19], off nt
	global_load_dwordx4 v[6:9], v[18:19], off offset:1024 nt
	global_load_dwordx4 v[10:13], v[18:19], off offset:2048 nt
	global_load_dwordx4 v[14:17], v[18:19], off offset:3072 nt
	s_nop 0
	global_load_dwordx4 v[18:21], v[34:35], off nt
	global_load_dwordx4 v[22:25], v[34:35], off offset:1024 nt
	global_load_dwordx4 v[26:29], v[34:35], off offset:2048 nt
	global_load_dwordx4 v[30:33], v[34:35], off offset:3072 nt
	v_lshlrev_b64 v[34:35], 10, v[62:63]
	v_mbcnt_hi_u32_b32 v63, -1, v36
	v_and_or_b32 v36, v63, 64, v65
	v_lshlrev_b32_e32 v107, 2, v36
	ds_bpermute_b32 v38, v107, v60
	ds_bpermute_b32 v40, v107, v60 offset:32
	v_lshl_add_u64 v[46:47], s[12:13], 0, v[66:67]
	s_mov_b64 s[4:5], 0x200000
	v_lshl_add_u64 v[98:99], v[46:47], 0, s[4:5]
	v_lshl_add_u64 v[34:35], s[10:11], 0, v[34:35]
	s_waitcnt lgkmcnt(1)
	v_lshlrev_b32_e32 v38, 7, v38
	v_mov_b32_e32 v39, v69
	v_lshl_add_u64 v[34:35], v[34:35], 0, v[68:69]
	v_lshl_add_u64 v[48:49], v[98:99], 0, v[38:39]
	s_waitcnt lgkmcnt(0)
	v_lshlrev_b32_e32 v38, 7, v40
	global_load_dwordx4 v[34:37], v[34:35], off nt
	v_lshl_add_u64 v[50:51], v[98:99], 0, v[38:39]
	global_load_dwordx4 v[38:41], v[48:49], off
	global_load_dwordx4 v[42:45], v[50:51], off
	ds_bpermute_b32 v48, v107, v60 offset:64
	ds_bpermute_b32 v49, v107, v60 offset:96
	s_mov_b64 s[4:5], 0x81a800
	v_lshl_add_u64 v[100:101], v[46:47], 0, s[4:5]
	v_mov_b32_e32 v47, v69
	s_waitcnt lgkmcnt(1)
	v_lshlrev_b32_e32 v46, 7, v48
	v_lshl_add_u64 v[92:93], v[100:101], 0, v[46:47]
	s_waitcnt lgkmcnt(0)
	v_lshlrev_b32_e32 v46, 7, v49
	v_lshl_add_u64 v[108:109], v[100:101], 0, v[46:47]
	v_lshl_add_u64 v[60:61], v[60:61], 2, v[96:97]
	global_load_dwordx4 v[46:49], v[92:93], off
	global_load_dwordx4 v[50:53], v[108:109], off
	v_or_b32_e32 v59, 0x1000, v0
	global_load_dword v108, v[60:61], off
	v_lshl_or_b32 v60, s2, 3, v1
	v_mov_b32_e32 v61, v69
	v_lshlrev_b64 v[60:61], 11, v[60:61]
	s_movk_i32 s3, 0x1220
	v_lshl_add_u64 v[60:61], s[14:15], 0, v[60:61]
	v_lshlrev_b32_e32 v92, 2, v70
	v_mov_b32_e32 v93, v69
	v_cmp_gt_u32_e64 s[4:5], s3, v59
	v_lshl_add_u64 v[60:61], v[60:61], 0, v[92:93]
	s_mov_b64 s[6:7], 0x2000000
	s_brev_b32 s3, 64
	v_lshl_add_u64 v[92:93], v[60:61], 0, s[6:7]
	v_add_co_u32_e64 v60, s[6:7], s3, v60
	s_nop 1
	v_addc_co_u32_e64 v61, s[6:7], 0, v61, s[6:7]
	s_waitcnt vmcnt(22)
	ds_write_b128 v58, v[72:75]
	s_waitcnt vmcnt(21)
	ds_write_b128 v58, v[76:79] offset:8192
	s_waitcnt vmcnt(20)
	ds_write_b128 v58, v[80:83] offset:16384
	s_waitcnt vmcnt(19)
	ds_write_b128 v58, v[84:87] offset:24576
	s_waitcnt vmcnt(18)
	ds_write_b128 v58, v[88:91] offset:32768
	s_waitcnt vmcnt(17)
	ds_write_b128 v58, v[102:105] offset:40960
	s_waitcnt vmcnt(16)
	ds_write_b128 v58, v[110:113] offset:49152
	s_waitcnt vmcnt(15)
	ds_write_b128 v58, v[114:117] offset:57344
	s_and_saveexec_b64 s[6:7], s[4:5]
	s_cbranch_execz .LBB1_2
	v_cndmask_b32_e64 v60, 0, v59, s[4:5]
	v_mov_b32_e32 v61, v69
	v_lshl_add_u64 v[60:61], v[60:61], 4, s[12:13]
	global_load_dwordx4 v[72:75], v[60:61], off
	v_lshlrev_b32_e32 v59, 4, v59
	s_waitcnt vmcnt(0)
	ds_write_b128 v59, v[72:75]
.LBB1_2:
	s_or_b64 exec, exec, s[6:7]
	s_and_saveexec_b64 s[4:5], vcc
	s_cbranch_execz .LBB1_4
	v_add_u32_e32 v59, 0x12000, v58
	s_waitcnt vmcnt(14)
	ds_write_b128 v59, v[54:57]
